# v37: v35 + ph6 parts merge: all four groups of a wave (first part, gate bytes, second part) fetched in front of the merge loop into four register sets picked by a counter; later parts fetched only whe
# baseline (speedup 1.0000x reference)
; __device__ __forceinline__ void ph6_hf(const Frame& F, const Args& A) {
;     ...
;     const int gw = F.vcu * NWAVES + F.wave, NGW = F.G * NWAVES, lane = F.lane;
;     const int mlo = (lane & 7) + ((lane & 8) ? 256 : 0);
; #pragma unroll 1
;     for (int g = gw; g < S_; g += NGW) {
;         const int h = g & 7, row0 = (g >> 3) * 8, blk = h * 32 + (row0 >> 8), rr0 = row0 & 255;
;         const int np = __builtin_amdgcn_readfirstlane(NPART[blk]);
;         const float* pm = PML + (size_t)blk * MAXP * 512 + rr0 + mlo; const bf16* po = PO + (size_t)blk * MAXP * 32768 + (size_t)rr0 * 128 + 2 * lane;
;         unsigned gz[8], ov[8]; float M[8], L[8]; f32x2_t a[8];
;         { const float ml = pm[0];
; #pragma unroll
;           for (int q = 0; q < 8; ++q) { ov[q] = *(const unsigned*)(po + q * 128); gz[q] = *(const unsigned short*)(A.ws + WS_Z8 + (size_t)(row0 + q) * pg8::Z8LD + 1024 + h * 128 + 2 * lane); }
.LBB0_968:
	v_readlane_b32 s0, v254, 4
	s_lshl_b32 s0, s0, 3
	v_readlane_b32 s1, v254, 32
	s_add_i32 s26, s0, s1
	v_readlane_b32 s88, v255, 20
	s_cmpk_gt_i32 s26, 0x1fff
	v_readlane_b32 s89, v255, 21
	s_cbranch_scc1 .LBB0_975
	s_add_u32 s27, s88, 0x70e00000
	s_addc_u32 s28, s89, 0
	s_add_u32 s29, s88, 0x90e00000
	s_addc_u32 s30, s89, 0
	v_lshlrev_b32_e32 v1, 5, v1
	v_and_b32_e32 v2, 7, v38
	s_movk_i32 s0, 0x100
	s_add_u32 s31, s88, 0x91600000
	v_and_or_b32 v8, v1, s0, v2
	v_mov_b32_e32 v35, 0
	v_readlane_b32 s0, v254, 0
	s_addc_u32 s33, s89, 0
	v_mov_b32_e32 v37, v35
	s_bfe_u32 s2, s0, 0x30006
	s_mov_b32 s1, 0
	v_lshl_add_u64 v[2:3], s[88:89], 0, v[36:37]
	s_lshl_b32 s0, s2, 8
	v_lshl_add_u64 v[2:3], v[2:3], 0, s[0:1]
	s_mov_b64 s[0:1], 0x9e00800
	s_lshl_b32 s34, s92, 3
	s_lshl_b32 s35, s2, 5
	s_lshl_b32 s36, s2, 7
	v_lshl_add_u64 v[2:3], v[2:3], 0, s[0:1]
	s_lshl_b32 s0, s2, 20
	s_add_u32 s0, s88, s0
	v_lshlrev_b32_e32 v4, 2, v8
	v_mov_b32_e32 v5, v35
	s_addc_u32 s1, s89, 0
	v_lshl_add_u64 v[4:5], s[0:1], 0, v[4:5]
	s_mov_b64 s[0:1], 0x90e00800
	v_lshl_add_u64 v[4:5], v[4:5], 0, s[0:1]
	s_lshl_b32 s0, s2, 25
	s_add_u32 s0, s88, s0
	s_addc_u32 s1, s89, 0
	v_lshl_add_u64 v[6:7], s[0:1], 0, v[36:37]
	s_mov_b64 s[0:1], 0x70e10400
	v_lshl_add_u64 v[6:7], v[6:7], 0, s[0:1]
	v_lshlrev_b32_e32 v1, 2, v8
	v_lshlrev_b32_e32 v42, 1, v34
	s_mov_b32 s37, 0xb2d00000
	s_mov_b64 s[0:1], 0x800
	s_mov_b64 s[2:3], 0x10000
	v_mov_b32_e32 v180, v42
	v_mov_b32_e32 v181, 0
	v_mov_b32_e32 v182, v1
	v_mov_b32_e32 v183, 0
	v_mov_b32_e32 v253, 0
	s_ashr_i32 s20, s26, 8
	s_add_i32 s4, s20, s35
	s_ashr_i32 s5, s4, 31
	s_and_b32 s14, s26, -8
	s_and_b32 s10, s26, 0xf8
	s_lshl_b64 s[6:7], s[4:5], 2
	s_add_u32 s6, s31, s6
	s_addc_u32 s7, s33, s7
	v_mov_b64_e32 v[170:171], s[6:7]
	s_lshl_b64 s[6:7], s[4:5], 15
	s_add_u32 s6, s29, s6
	s_addc_u32 s7, s30, s7
	s_lshl_b32 s8, s10, 2
	s_add_u32 s8, s6, s8
	s_addc_u32 s9, s7, 0
	s_lshl_b64 s[4:5], s[4:5], 20
	s_add_u32 s4, s27, s4
	s_addc_u32 s5, s28, s5
	s_lshl_b32 s6, s10, 8
	s_add_u32 s6, s4, s6
	s_addc_u32 s7, s5, 0
	s_mul_i32 s5, s14, 0x1800
	s_mul_hi_i32 s4, s14, 0x1800
	s_add_u32 s5, s88, s5
	v_lshl_add_u64 v[172:173], s[8:9], 0, v[182:183]
	s_addc_u32 s8, s89, s4
	s_add_u32 s4, s5, s36
	s_addc_u32 s5, s8, 0
	s_or_b32 s18, s14, 1
	v_lshl_add_u64 v[8:9], s[4:5], 0, v[34:35]
	s_mul_i32 s5, s18, 0x1800
	s_mul_hi_i32 s4, s18, 0x1800
	s_add_u32 s5, s88, s5
	s_addc_u32 s8, s89, s4
	s_add_u32 s4, s5, s36
	s_addc_u32 s5, s8, 0
	s_or_b32 s16, s14, 2
	v_lshl_add_u64 v[10:11], s[4:5], 0, v[34:35]
	s_mul_i32 s5, s16, 0x1800
	s_mul_hi_i32 s4, s16, 0x1800
	s_add_u32 s5, s88, s5
	s_addc_u32 s8, s89, s4
	s_add_u32 s4, s5, s36
	s_addc_u32 s5, s8, 0
	s_or_b32 s12, s14, 3
	v_lshl_add_u64 v[12:13], s[4:5], 0, v[34:35]
	s_mul_i32 s5, s12, 0x1800
	s_mul_hi_i32 s4, s12, 0x1800
	s_add_u32 s5, s88, s5
	s_addc_u32 s8, s89, s4
	s_add_u32 s4, s5, s36
	s_addc_u32 s5, s8, 0
	s_or_b32 s10, s14, 4
	v_lshl_add_u64 v[14:15], s[4:5], 0, v[34:35]
	s_mul_i32 s5, s10, 0x1800
	s_mul_hi_i32 s4, s10, 0x1800
	s_add_u32 s5, s88, s5
	s_addc_u32 s8, s89, s4
	s_add_u32 s4, s5, s36
	s_addc_u32 s5, s8, 0
	s_or_b32 s8, s14, 5
	v_add_co_u32_e32 v8, vcc, s37, v8
	v_lshl_add_u64 v[16:17], s[4:5], 0, v[34:35]
	s_mul_i32 s5, s8, 0x1800
	v_addc_co_u32_e32 v9, vcc, 0, v9, vcc
	s_mul_hi_i32 s4, s8, 0x1800
	s_add_u32 s5, s88, s5
	v_add_co_u32_e32 v10, vcc, s37, v10
	s_addc_u32 s9, s89, s4
	s_nop 0
	v_addc_co_u32_e32 v11, vcc, 0, v11, vcc
	s_add_u32 s4, s5, s36
	v_add_co_u32_e32 v12, vcc, s37, v12
	s_addc_u32 s5, s9, 0
	s_nop 0
	v_addc_co_u32_e32 v13, vcc, 0, v13, vcc
	v_lshl_add_u64 v[18:19], s[4:5], 0, v[34:35]
	s_or_b32 s4, s14, 6
	v_add_co_u32_e32 v14, vcc, s37, v14
	s_mul_i32 s9, s4, 0x1800
	s_nop 0
	v_addc_co_u32_e32 v15, vcc, 0, v15, vcc
	s_mul_hi_i32 s5, s4, 0x1800
	s_add_u32 s9, s88, s9
	v_add_co_u32_e32 v16, vcc, s37, v16
	s_addc_u32 s5, s89, s5
	s_nop 0
	v_addc_co_u32_e32 v17, vcc, 0, v17, vcc
	s_add_u32 s22, s9, s36
	v_add_co_u32_e32 v18, vcc, s37, v18
	s_addc_u32 s23, s5, 0
	s_nop 0
	v_addc_co_u32_e32 v19, vcc, 0, v19, vcc
	v_lshl_add_u64 v[20:21], s[22:23], 0, v[34:35]
	v_add_co_u32_e32 v20, vcc, s37, v20
	v_addc_co_u32_e32 v21, vcc, 0, v21, vcc
	v_mov_b64_e32 v[176:177], v[8:9]
	v_lshl_add_u64 v[174:175], s[6:7], 0, v[180:181]
	s_or_b32 s6, s26, 7
	s_mul_i32 s7, s6, 0x1800
	s_mul_hi_i32 s5, s6, 0x1800
	s_add_u32 s7, s88, s7
	s_addc_u32 s5, s89, s5
	s_add_u32 s22, s7, s36
	s_addc_u32 s23, s5, 0
	v_lshl_add_u64 v[8:9], s[22:23], 0, v[34:35]
	v_add_co_u32_e32 v8, vcc, s37, v8
	s_nop 1
	v_addc_co_u32_e32 v9, vcc, 0, v9, vcc
	s_lshl_b32 s98, s20, 15
	s_lshl_b32 s99, s26, 2
	s_and_b32 s99, s99, 0x3e0
	s_or_b32 s98, s98, s99
	s_mov_b32 s99, 0
	v_lshl_add_u64 v[210:211], v[4:5], 0, s[98:99]
	s_lshl_b32 s98, s20, 20
	s_lshl_b32 s99, s26, 8
	s_and_b32 s99, s99, 0xf800
	s_or_b32 s98, s98, s99
	s_mov_b32 s99, 0
	v_lshl_add_u64 v[212:213], v[6:7], 0, s[98:99]
	global_load_dword v100, v[170:171], off
	global_load_dword v101, v[172:173], off
	global_load_dword v118, v[210:211], off
	global_load_dword v102, v[174:175], off
	global_load_dword v103, v[174:175], off offset:256
	global_load_dword v104, v[174:175], off offset:512
	global_load_dword v105, v[174:175], off offset:768
	global_load_dword v106, v[174:175], off offset:1024
	global_load_dword v107, v[174:175], off offset:1280
	global_load_dword v108, v[174:175], off offset:1536
	global_load_dword v116, v[174:175], off offset:1792
	global_load_dword v119, v[212:213], off offset:-1024
	global_load_dword v120, v[212:213], off offset:-768
	global_load_dword v121, v[212:213], off offset:-512
	global_load_dword v122, v[212:213], off offset:-256
; __device__ __forceinline__ void ph6_hf(const Frame& F, const Args& A) {
;     ...
;         const int np = __builtin_amdgcn_readfirstlane(NPART[blk]);
;         const float* pm = PML + (size_t)blk * MAXP * 512 + rr0 + mlo; const bf16* po = PO + (size_t)blk * MAXP * 32768 + (size_t)rr0 * 128 + 2 * lane;
;         unsigned gz[8], ov[8]; float M[8], L[8]; f32x2_t a[8];
;         { const float ml = pm[0];
; #pragma unroll
;           for (int q = 0; q < 8; ++q) { ov[q] = *(const unsigned*)(po + q * 128); gz[q] = *(const unsigned short*)(A.ws + WS_Z8 + (size_t)(row0 + q) * pg8::Z8LD + 1024 + h * 128 + 2 * lane); }
	global_load_dword v123, v[212:213], off
	global_load_dword v124, v[212:213], off offset:256
	global_load_dword v125, v[212:213], off offset:512
	global_load_dword v126, v[212:213], off offset:768
	global_load_ushort v109, v[176:177], off offset:1024
	global_load_ushort v110, v[10:11], off offset:1024
	global_load_ushort v111, v[12:13], off offset:1024
	global_load_ushort v112, v[14:15], off offset:1024
	global_load_ushort v113, v[16:17], off offset:1024
	global_load_ushort v114, v[18:19], off offset:1024
	global_load_ushort v115, v[20:21], off offset:1024
	global_load_ushort v117, v[8:9], off offset:1024
	global_load_dword v127, v[170:171], off offset:32
	s_mov_b32 s98, 0x40000
	s_mov_b32 s99, 0
	v_lshl_add_u64 v[178:179], v[172:173], 0, s[98:99]
	global_load_dword v128, v[178:179], off
	v_lshl_add_u64 v[178:179], v[210:211], 0, s[98:99]
	global_load_dword v145, v[178:179], off
	s_mov_b32 s98, 0x800000
	v_lshl_add_u64 v[178:179], v[174:175], 0, s[98:99]
	global_load_dword v129, v[178:179], off
	global_load_dword v130, v[178:179], off offset:256
	global_load_dword v131, v[178:179], off offset:512
	global_load_dword v132, v[178:179], off offset:768
	global_load_dword v133, v[178:179], off offset:1024
	global_load_dword v134, v[178:179], off offset:1280
	global_load_dword v135, v[178:179], off offset:1536
	global_load_dword v143, v[178:179], off offset:1792
	v_lshl_add_u64 v[178:179], v[212:213], 0, s[98:99]
	global_load_dword v146, v[178:179], off offset:-1024
	global_load_dword v147, v[178:179], off offset:-768
	global_load_dword v148, v[178:179], off offset:-512
	global_load_dword v149, v[178:179], off offset:-256
	global_load_dword v150, v[178:179], off
	global_load_dword v151, v[178:179], off offset:256
	global_load_dword v152, v[178:179], off offset:512
	global_load_dword v153, v[178:179], off offset:768
	s_mov_b32 s98, 0xc00000
	v_lshl_add_u64 v[178:179], v[176:177], 0, s[98:99]
	global_load_ushort v136, v[178:179], off offset:1024
	v_lshl_add_u64 v[178:179], v[10:11], 0, s[98:99]
	global_load_ushort v137, v[178:179], off offset:1024
	v_lshl_add_u64 v[178:179], v[12:13], 0, s[98:99]
	global_load_ushort v138, v[178:179], off offset:1024
	v_lshl_add_u64 v[178:179], v[14:15], 0, s[98:99]
	global_load_ushort v139, v[178:179], off offset:1024
	v_lshl_add_u64 v[178:179], v[16:17], 0, s[98:99]
	global_load_ushort v140, v[178:179], off offset:1024
	v_lshl_add_u64 v[178:179], v[18:19], 0, s[98:99]
	global_load_ushort v141, v[178:179], off offset:1024
	v_lshl_add_u64 v[178:179], v[20:21], 0, s[98:99]
	global_load_ushort v142, v[178:179], off offset:1024
	v_lshl_add_u64 v[178:179], v[8:9], 0, s[98:99]
	global_load_ushort v144, v[178:179], off offset:1024
	global_load_dword v154, v[170:171], off offset:64
	s_mov_b32 s98, 0x80000
	s_mov_b32 s99, 0
	v_lshl_add_u64 v[178:179], v[172:173], 0, s[98:99]
	global_load_dword v155, v[178:179], off
	v_lshl_add_u64 v[178:179], v[210:211], 0, s[98:99]
	global_load_dword v188, v[178:179], off
	s_mov_b32 s98, 0x1000000
	v_lshl_add_u64 v[178:179], v[174:175], 0, s[98:99]
	global_load_dword v156, v[178:179], off
	global_load_dword v157, v[178:179], off offset:256
	global_load_dword v158, v[178:179], off offset:512
	global_load_dword v159, v[178:179], off offset:768
	global_load_dword v160, v[178:179], off offset:1024
	global_load_dword v161, v[178:179], off offset:1280
	global_load_dword v162, v[178:179], off offset:1536
	global_load_dword v186, v[178:179], off offset:1792
	v_lshl_add_u64 v[178:179], v[212:213], 0, s[98:99]
	global_load_dword v189, v[178:179], off offset:-1024
	global_load_dword v190, v[178:179], off offset:-768
	global_load_dword v191, v[178:179], off offset:-512
	global_load_dword v192, v[178:179], off offset:-256
	global_load_dword v193, v[178:179], off
	global_load_dword v194, v[178:179], off offset:256
	global_load_dword v195, v[178:179], off offset:512
	global_load_dword v196, v[178:179], off offset:768
	s_mov_b32 s98, 0x1800000
	v_lshl_add_u64 v[178:179], v[176:177], 0, s[98:99]
	global_load_ushort v163, v[178:179], off offset:1024
	v_lshl_add_u64 v[178:179], v[10:11], 0, s[98:99]
	global_load_ushort v164, v[178:179], off offset:1024
	v_lshl_add_u64 v[178:179], v[12:13], 0, s[98:99]
	global_load_ushort v165, v[178:179], off offset:1024
	v_lshl_add_u64 v[178:179], v[14:15], 0, s[98:99]
	global_load_ushort v166, v[178:179], off offset:1024
	v_lshl_add_u64 v[178:179], v[16:17], 0, s[98:99]
	global_load_ushort v167, v[178:179], off offset:1024
	v_lshl_add_u64 v[178:179], v[18:19], 0, s[98:99]
	global_load_ushort v168, v[178:179], off offset:1024
	v_lshl_add_u64 v[178:179], v[20:21], 0, s[98:99]
	global_load_ushort v169, v[178:179], off offset:1024
	v_lshl_add_u64 v[178:179], v[8:9], 0, s[98:99]
	global_load_ushort v187, v[178:179], off offset:1024
	global_load_dword v197, v[170:171], off offset:96
	s_mov_b32 s98, 0xc0000
	s_mov_b32 s99, 0
	v_lshl_add_u64 v[178:179], v[172:173], 0, s[98:99]
	global_load_dword v198, v[178:179], off
	v_lshl_add_u64 v[178:179], v[210:211], 0, s[98:99]
	global_load_dword v229, v[178:179], off
	s_mov_b32 s98, 0x1800000
	v_lshl_add_u64 v[178:179], v[174:175], 0, s[98:99]
	global_load_dword v199, v[178:179], off
	global_load_dword v214, v[178:179], off offset:256
	global_load_dword v215, v[178:179], off offset:512
	global_load_dword v216, v[178:179], off offset:768
	global_load_dword v217, v[178:179], off offset:1024
	global_load_dword v218, v[178:179], off offset:1280
	global_load_dword v219, v[178:179], off offset:1536
	global_load_dword v227, v[178:179], off offset:1792
	v_lshl_add_u64 v[178:179], v[212:213], 0, s[98:99]
	global_load_dword v230, v[178:179], off offset:-1024
	global_load_dword v231, v[178:179], off offset:-768
	global_load_dword v232, v[178:179], off offset:-512
	global_load_dword v233, v[178:179], off offset:-256
	global_load_dword v234, v[178:179], off
	global_load_dword v235, v[178:179], off offset:256
	global_load_dword v236, v[178:179], off offset:512
	global_load_dword v237, v[178:179], off offset:768
	s_mov_b32 s98, 0x2400000
	v_lshl_add_u64 v[178:179], v[176:177], 0, s[98:99]
	global_load_ushort v220, v[178:179], off offset:1024
	v_lshl_add_u64 v[178:179], v[10:11], 0, s[98:99]
	global_load_ushort v221, v[178:179], off offset:1024
	v_lshl_add_u64 v[178:179], v[12:13], 0, s[98:99]
	global_load_ushort v222, v[178:179], off offset:1024
	v_lshl_add_u64 v[178:179], v[14:15], 0, s[98:99]
	global_load_ushort v223, v[178:179], off offset:1024
	v_lshl_add_u64 v[178:179], v[16:17], 0, s[98:99]
	global_load_ushort v224, v[178:179], off offset:1024
	v_lshl_add_u64 v[178:179], v[18:19], 0, s[98:99]
	global_load_ushort v225, v[178:179], off offset:1024
	v_lshl_add_u64 v[178:179], v[20:21], 0, s[98:99]
	global_load_ushort v226, v[178:179], off offset:1024
	v_lshl_add_u64 v[178:179], v[8:9], 0, s[98:99]
	global_load_ushort v228, v[178:179], off offset:1024
	s_branch .LBB0_972

; __device__ __forceinline__ float rdl(float v, int l) { return __builtin_bit_cast(float, __builtin_amdgcn_readlane(__builtin_bit_cast(int, v), l)); }
; __device__ __forceinline__ void ph6_hf(const Frame& F, const Args& A) {
;     ...
;     for (int g = gw; g < S_; g += NGW) {
;         const int h = g & 7, row0 = (g >> 3) * 8, blk = h * 32 + (row0 >> 8), rr0 = row0 & 255;
;         const int np = __builtin_amdgcn_readfirstlane(NPART[blk]);
;         const float* pm = PML + (size_t)blk * MAXP * 512 + rr0 + mlo; const bf16* po = PO + (size_t)blk * MAXP * 32768 + (size_t)rr0 * 128 + 2 * lane;
;         unsigned gz[8], ov[8]; float M[8], L[8]; f32x2_t a[8];
;         { const float ml = pm[0];
; #pragma unroll
;           for (int q = 0; q < 8; ++q) { ov[q] = *(const unsigned*)(po + q * 128); gz[q] = *(const unsigned short*)(A.ws + WS_Z8 + (size_t)(row0 + q) * pg8::Z8LD + 1024 + h * 128 + 2 * lane); }
; #pragma unroll
;           for (int q = 0; q < 8; ++q) { M[q] = rdl(ml, q); L[q] = rdl(ml, 8 + q); a[q].x = bflo(ov[q]); a[q].y = bfhi(ov[q]); } }
.LBB0_972:
	s_ashr_i32 s20, s26, 8
	s_add_i32 s4, s20, s35
	s_ashr_i32 s5, s4, 31
	s_and_b32 s14, s26, -8
	s_and_b32 s10, s26, 0xf8
	s_lshl_b64 s[6:7], s[4:5], 2
	s_add_u32 s6, s31, s6
	s_addc_u32 s7, s33, s7
	s_lshl_b64 s[6:7], s[4:5], 15
	s_add_u32 s6, s29, s6
	s_addc_u32 s7, s30, s7
	s_lshl_b32 s8, s10, 2
	s_add_u32 s8, s6, s8
	s_addc_u32 s9, s7, 0
	s_lshl_b64 s[4:5], s[4:5], 20
	s_add_u32 s4, s27, s4
	s_addc_u32 s5, s28, s5
	s_lshl_b32 s6, s10, 8
	s_add_u32 s6, s4, s6
	s_addc_u32 s7, s5, 0
	s_mul_i32 s5, s14, 0x1800
	s_mul_hi_i32 s4, s14, 0x1800
	s_add_u32 s5, s88, s5
	s_addc_u32 s8, s89, s4
	s_add_u32 s4, s5, s36
	s_addc_u32 s5, s8, 0
	s_or_b32 s18, s14, 1
	v_lshl_add_u64 v[8:9], s[4:5], 0, v[34:35]
	s_mul_i32 s5, s18, 0x1800
	s_mul_hi_i32 s4, s18, 0x1800
	s_add_u32 s5, s88, s5
	s_addc_u32 s8, s89, s4
	s_add_u32 s4, s5, s36
	s_addc_u32 s5, s8, 0
	s_or_b32 s16, s14, 2
	v_lshl_add_u64 v[10:11], s[4:5], 0, v[34:35]
	s_mul_i32 s5, s16, 0x1800
	s_mul_hi_i32 s4, s16, 0x1800
	s_add_u32 s5, s88, s5
	s_addc_u32 s8, s89, s4
	s_add_u32 s4, s5, s36
	s_addc_u32 s5, s8, 0
	s_or_b32 s12, s14, 3
	v_lshl_add_u64 v[12:13], s[4:5], 0, v[34:35]
	s_mul_i32 s5, s12, 0x1800
	s_mul_hi_i32 s4, s12, 0x1800
	s_add_u32 s5, s88, s5
	s_addc_u32 s8, s89, s4
	s_add_u32 s4, s5, s36
	s_addc_u32 s5, s8, 0
	s_or_b32 s10, s14, 4
	v_lshl_add_u64 v[14:15], s[4:5], 0, v[34:35]
	s_mul_i32 s5, s10, 0x1800
	s_mul_hi_i32 s4, s10, 0x1800
	s_add_u32 s5, s88, s5
	s_addc_u32 s8, s89, s4
	s_add_u32 s4, s5, s36
	s_addc_u32 s5, s8, 0
	s_or_b32 s8, s14, 5
	v_add_co_u32_e32 v8, vcc, s37, v8
	v_lshl_add_u64 v[16:17], s[4:5], 0, v[34:35]
	s_mul_i32 s5, s8, 0x1800
	v_addc_co_u32_e32 v9, vcc, 0, v9, vcc
	s_mul_hi_i32 s4, s8, 0x1800
	s_add_u32 s5, s88, s5
	v_add_co_u32_e32 v10, vcc, s37, v10
	s_addc_u32 s9, s89, s4
	s_nop 0
	v_addc_co_u32_e32 v11, vcc, 0, v11, vcc
	s_add_u32 s4, s5, s36
	v_add_co_u32_e32 v12, vcc, s37, v12
	s_addc_u32 s5, s9, 0
	s_nop 0
	v_addc_co_u32_e32 v13, vcc, 0, v13, vcc
	v_lshl_add_u64 v[18:19], s[4:5], 0, v[34:35]
	s_or_b32 s4, s14, 6
	v_add_co_u32_e32 v14, vcc, s37, v14
	s_mul_i32 s9, s4, 0x1800
	s_nop 0
	v_addc_co_u32_e32 v15, vcc, 0, v15, vcc
	s_mul_hi_i32 s5, s4, 0x1800
	s_add_u32 s9, s88, s9
	v_add_co_u32_e32 v16, vcc, s37, v16
	s_addc_u32 s5, s89, s5
	s_nop 0
	v_addc_co_u32_e32 v17, vcc, 0, v17, vcc
	s_add_u32 s22, s9, s36
	v_add_co_u32_e32 v18, vcc, s37, v18
	s_addc_u32 s23, s5, 0
	s_nop 0
	v_addc_co_u32_e32 v19, vcc, 0, v19, vcc
	v_lshl_add_u64 v[20:21], s[22:23], 0, v[34:35]
	v_add_co_u32_e32 v20, vcc, s37, v20
	v_addc_co_u32_e32 v21, vcc, 0, v21, vcc
	s_or_b32 s6, s26, 7
	s_mul_i32 s7, s6, 0x1800
	s_mul_hi_i32 s5, s6, 0x1800
	s_add_u32 s7, s88, s7
	s_addc_u32 s5, s89, s5
	s_add_u32 s22, s7, s36
	s_addc_u32 s23, s5, 0
	v_lshl_add_u64 v[8:9], s[22:23], 0, v[34:35]
	v_add_co_u32_e32 v8, vcc, s37, v8
	s_nop 1
	v_addc_co_u32_e32 v9, vcc, 0, v9, vcc
	v_readfirstlane_b32 s98, v253
	v_add_u32_e32 v253, 1, v253
	s_cmp_eq_u32 s98, 0
	s_cbranch_scc1 .Lhf_s0
	s_cmp_eq_u32 s98, 1
	s_cbranch_scc1 .Lhf_s1
	s_cmp_eq_u32 s98, 2
	s_cbranch_scc1 .Lhf_s2
	s_waitcnt vmcnt(24)
	v_mov_b32_e32 v22, v197
	v_mov_b32_e32 v23, v198
	v_mov_b32_e32 v24, v199
	v_mov_b32_e32 v25, v214
	v_mov_b32_e32 v27, v215
	v_mov_b32_e32 v30, v216
	v_mov_b32_e32 v31, v217
	v_mov_b32_e32 v36, v218
	v_mov_b32_e32 v37, v219
	v_mov_b32_e32 v48, v220
	v_mov_b32_e32 v49, v221
	v_mov_b32_e32 v50, v222
	v_mov_b32_e32 v44, v223
	v_mov_b32_e32 v45, v224
	v_mov_b32_e32 v46, v225
	v_mov_b32_e32 v43, v226
	v_mov_b32_e32 v10, v227
	v_mov_b32_e32 v47, v228
	v_mov_b32_e32 v200, v229
	v_mov_b32_e32 v201, v230
	v_mov_b32_e32 v202, v231
	v_mov_b32_e32 v203, v232
	v_mov_b32_e32 v204, v233
	v_mov_b32_e32 v205, v234
	v_mov_b32_e32 v206, v235
	v_mov_b32_e32 v207, v236
	v_mov_b32_e32 v208, v237
	s_branch .Lhf_go
.Lhf_s2:
	s_waitcnt vmcnt(43)
	v_mov_b32_e32 v22, v154
	v_mov_b32_e32 v23, v155
	v_mov_b32_e32 v24, v156
	v_mov_b32_e32 v25, v157
	v_mov_b32_e32 v27, v158
	v_mov_b32_e32 v30, v159
	v_mov_b32_e32 v31, v160
	v_mov_b32_e32 v36, v161
	v_mov_b32_e32 v37, v162
	v_mov_b32_e32 v48, v163
	v_mov_b32_e32 v49, v164
	v_mov_b32_e32 v50, v165
	v_mov_b32_e32 v44, v166
	v_mov_b32_e32 v45, v167
	v_mov_b32_e32 v46, v168
	v_mov_b32_e32 v43, v169
	v_mov_b32_e32 v10, v186
	v_mov_b32_e32 v47, v187
	v_mov_b32_e32 v200, v188
	v_mov_b32_e32 v201, v189
	v_mov_b32_e32 v202, v190
	v_mov_b32_e32 v203, v191
	v_mov_b32_e32 v204, v192
	v_mov_b32_e32 v205, v193
	v_mov_b32_e32 v206, v194
	v_mov_b32_e32 v207, v195
	v_mov_b32_e32 v208, v196
	s_branch .Lhf_go
.Lhf_s1:
	s_waitcnt vmcnt(62)
	v_mov_b32_e32 v22, v127
	v_mov_b32_e32 v23, v128
	v_mov_b32_e32 v24, v129
	v_mov_b32_e32 v25, v130
	v_mov_b32_e32 v27, v131
	v_mov_b32_e32 v30, v132
	v_mov_b32_e32 v31, v133
	v_mov_b32_e32 v36, v134
	v_mov_b32_e32 v37, v135
	v_mov_b32_e32 v48, v136
	v_mov_b32_e32 v49, v137
	v_mov_b32_e32 v50, v138
	v_mov_b32_e32 v44, v139
	v_mov_b32_e32 v45, v140
	v_mov_b32_e32 v46, v141
	v_mov_b32_e32 v43, v142
	v_mov_b32_e32 v10, v143
	v_mov_b32_e32 v47, v144
	v_mov_b32_e32 v200, v145
	v_mov_b32_e32 v201, v146
	v_mov_b32_e32 v202, v147
	v_mov_b32_e32 v203, v148
	v_mov_b32_e32 v204, v149
	v_mov_b32_e32 v205, v150
	v_mov_b32_e32 v206, v151
	v_mov_b32_e32 v207, v152
	v_mov_b32_e32 v208, v153
	s_branch .Lhf_go
.Lhf_s0:
	s_waitcnt vmcnt(54)
	v_mov_b32_e32 v22, v100
	v_mov_b32_e32 v23, v101
	v_mov_b32_e32 v24, v102
	v_mov_b32_e32 v25, v103
	v_mov_b32_e32 v27, v104
	v_mov_b32_e32 v30, v105
	v_mov_b32_e32 v31, v106
	v_mov_b32_e32 v36, v107
	v_mov_b32_e32 v37, v108
	v_mov_b32_e32 v48, v109
	v_mov_b32_e32 v49, v110
	v_mov_b32_e32 v50, v111
	v_mov_b32_e32 v44, v112
	v_mov_b32_e32 v45, v113
	v_mov_b32_e32 v46, v114
	v_mov_b32_e32 v43, v115
	v_mov_b32_e32 v10, v116
	v_mov_b32_e32 v47, v117
	v_mov_b32_e32 v200, v118
	v_mov_b32_e32 v201, v119
	v_mov_b32_e32 v202, v120
	v_mov_b32_e32 v203, v121
	v_mov_b32_e32 v204, v122
	v_mov_b32_e32 v205, v123
	v_mov_b32_e32 v206, v124
	v_mov_b32_e32 v207, v125
	v_mov_b32_e32 v208, v126
; __device__ __forceinline__ float rdl(float v, int l) { return __builtin_bit_cast(float, __builtin_amdgcn_readlane(__builtin_bit_cast(int, v), l)); }
; __device__ __forceinline__ void ph6_hf(const Frame& F, const Args& A) {
;     ...
;           for (int q = 0; q < 8; ++q) { M[q] = rdl(ml, q); L[q] = rdl(ml, 8 + q); a[q].x = bflo(ov[q]); a[q].y = bfhi(ov[q]); } }
; #pragma unroll 1
;         for (int p = 1; p < np; ++p) { const float ml = pm[(size_t)p * 512];
; #pragma unroll
;             for (int q = 0; q < 8; ++q) ov[q] = *(const unsigned*)(po + (size_t)p * 32768 + q * 128);
; #pragma unroll
;             for (int q = 0; q < 8; ++q) { const float mp = rdl(ml, q), lp = rdl(ml, 8 + q);
;                 const float Mn = fmaxf(M[q], mp), w0 = __builtin_amdgcn_exp2f((M[q] - Mn) * C2), w1 = __builtin_amdgcn_exp2f((mp - Mn) * C2);
;                 L[q] = L[q] * w0 + lp * w1; a[q].x = a[q].x * w0 + bflo(ov[q]) * w1; a[q].y = a[q].y * w0 + bfhi(ov[q]) * w1; M[q] = Mn; } }
.Lhf_go:
	v_readfirstlane_b32 s5, v22
	v_readlane_b32 s7, v23, 0
	v_readlane_b32 s11, v23, 8
	v_lshlrev_b32_e32 v32, 16, v24
	v_and_b32_e32 v33, 0xffff0000, v24
	v_readlane_b32 s9, v23, 1
	v_readlane_b32 s15, v23, 9
	v_readlane_b32 s13, v23, 2
	v_readlane_b32 s19, v23, 10
	v_readlane_b32 s17, v23, 3
	v_readlane_b32 s23, v23, 11
	v_readlane_b32 s22, v23, 4
	v_readlane_b32 s25, v23, 12
	v_readlane_b32 s24, v23, 5
	v_readlane_b32 s39, v23, 13
	v_readlane_b32 s38, v23, 6
	v_readlane_b32 s41, v23, 14
	v_readlane_b32 s40, v23, 7
	v_readlane_b32 s42, v23, 15
	s_cmp_lt_i32 s5, 2
	v_lshlrev_b32_e32 v28, 16, v25
	v_and_b32_e32 v29, 0xffff0000, v25
	v_lshlrev_b32_e32 v26, 16, v27
	v_and_b32_e32 v27, 0xffff0000, v27
	v_lshlrev_b32_e32 v24, 16, v30
	v_and_b32_e32 v25, 0xffff0000, v30
	v_lshlrev_b32_e32 v18, 16, v31
	v_and_b32_e32 v19, 0xffff0000, v31
	v_lshlrev_b32_e32 v16, 16, v36
	v_and_b32_e32 v17, 0xffff0000, v36
	v_lshlrev_b32_e32 v12, 16, v37
	v_and_b32_e32 v13, 0xffff0000, v37
	v_lshlrev_b32_e32 v8, 16, v10
	v_and_b32_e32 v10, 0xffff0000, v10
	s_cbranch_scc1 .LBB0_970
	s_lshl_b32 s21, s26, 2
	s_and_b32 s43, s21, 0x3e0
	s_lshl_b32 s21, s26, 8
	s_and_b32 s46, s21, 0xf800
	s_ashr_i32 s21, s20, 31
	s_lshl_b64 s[44:45], s[20:21], 15
	s_lshl_b64 s[20:21], s[20:21], 20
	s_or_b32 s44, s44, s43
	s_or_b32 s20, s20, s46
	s_add_i32 s5, s5, -1
	v_lshl_add_u64 v[38:39], v[4:5], 0, s[44:45]
	v_lshl_add_u64 v[40:41], v[6:7], 0, s[20:21]
	v_mov_b32_e32 v14, s42
	v_mov_b32_e32 v20, s41
	v_mov_b32_e32 v23, s39
	v_mov_b32_e32 v22, s25
	v_mov_b32_e32 v31, s23
	v_mov_b32_e32 v30, s19
	v_mov_b32_e32 v37, s15
	v_mov_b32_e32 v36, s11
	v_mov_b32_e32 v51, s40
	v_mov_b32_e32 v52, s38
	v_mov_b32_e32 v53, s24
	v_mov_b32_e32 v54, s22
	v_mov_b32_e32 v55, s17
	v_mov_b32_e32 v56, s13
	v_mov_b32_e32 v57, s9
	v_mov_b32_e32 v58, s7
.LBB0_974:
	v_mov_b32_e32 v9, v200
	v_mov_b32_e32 v11, v201
	v_mov_b32_e32 v15, v202
	v_mov_b32_e32 v21, v203
	v_mov_b32_e32 v59, v204
	v_mov_b32_e32 v69, v205
	v_mov_b32_e32 v71, v206
	v_mov_b32_e32 v73, v207
	v_mov_b32_e32 v74, v208
	v_max_f32_e32 v75, v58, v58
	v_max_f32_e32 v76, v57, v57
	v_max_f32_e32 v77, v56, v56
	v_max_f32_e32 v79, v54, v54
	v_max_f32_e32 v78, v55, v55
	v_max_f32_e32 v80, v53, v53
	v_max_f32_e32 v81, v52, v52
	v_max_f32_e32 v82, v51, v51
	s_add_i32 s5, s5, -1
	v_lshl_add_u64 v[38:39], v[38:39], 0, s[0:1]
	v_lshl_add_u64 v[40:41], v[40:41], 0, s[2:3]
	s_cmp_eq_u32 s5, 0
	s_cbranch_scc1 .Lhf_last
	global_load_dword v200, v[38:39], off
	global_load_dword v201, v[40:41], off offset:-1024
	global_load_dword v202, v[40:41], off offset:-768
	global_load_dword v203, v[40:41], off offset:-512
	global_load_dword v204, v[40:41], off offset:-256
	global_load_dword v205, v[40:41], off
	global_load_dword v206, v[40:41], off offset:256
	global_load_dword v207, v[40:41], off offset:512
	global_load_dword v208, v[40:41], off offset:768
; __device__ __forceinline__ float rdl(float v, int l) { return __builtin_bit_cast(float, __builtin_amdgcn_readlane(__builtin_bit_cast(int, v), l)); }
; __device__ __forceinline__ void ph6_hf(const Frame& F, const Args& A) {
;     ...
;             for (int q = 0; q < 8; ++q) { const float mp = rdl(ml, q), lp = rdl(ml, 8 + q);
;                 const float Mn = fmaxf(M[q], mp), w0 = __builtin_amdgcn_exp2f((M[q] - Mn) * C2), w1 = __builtin_amdgcn_exp2f((mp - Mn) * C2);
;                 L[q] = L[q] * w0 + lp * w1; a[q].x = a[q].x * w0 + bflo(ov[q]) * w1; a[q].y = a[q].y * w0 + bfhi(ov[q]) * w1; M[q] = Mn; } }
.Lhf_last:
	v_readlane_b32 s7, v9, 0
	v_readlane_b32 s9, v9, 1
	v_readlane_b32 s11, v9, 2
	v_readlane_b32 s15, v9, 4
	v_readlane_b32 s20, v9, 8
	v_lshlrev_b32_e32 v60, 16, v11
	v_and_b32_e32 v61, 0xffff0000, v11
	v_readlane_b32 s21, v9, 9
	v_readlane_b32 s22, v9, 10
	v_lshlrev_b32_e32 v64, 16, v21
	v_and_b32_e32 v65, 0xffff0000, v21
	v_readlane_b32 s13, v9, 3
	v_readlane_b32 s23, v9, 11
	v_lshlrev_b32_e32 v66, 16, v59
	v_and_b32_e32 v67, 0xffff0000, v59
	v_readlane_b32 s24, v9, 12
	v_readlane_b32 s17, v9, 5
	v_readlane_b32 s25, v9, 13
	v_readlane_b32 s19, v9, 6
	v_readlane_b32 s38, v9, 14
	v_readlane_b32 s39, v9, 7
	v_readlane_b32 s40, v9, 15
	v_lshlrev_b32_e32 v9, 16, v74
	v_and_b32_e32 v21, 0xffff0000, v74
	v_max_f32_e64 v11, s7, s7
	v_max_f32_e64 v59, s9, s9
	v_max_f32_e64 v74, s11, s11
	v_max_f32_e64 v84, s15, s15
	v_max_f32_e64 v83, s13, s13
	v_max_f32_e64 v85, s17, s17
	v_max_f32_e64 v86, s19, s19
	v_max_f32_e64 v87, s39, s39
	v_max_f32_e32 v11, v75, v11
	v_max_f32_e32 v59, v76, v59
	v_max_f32_e32 v74, v77, v74
	v_max_f32_e32 v76, v79, v84
	v_max_f32_e32 v75, v78, v83
	v_max_f32_e32 v77, v80, v85
	v_max_f32_e32 v78, v81, v86
	v_max_f32_e32 v79, v82, v87
	v_sub_f32_e32 v81, s7, v11
	v_sub_f32_e32 v83, s9, v59
	v_sub_f32_e32 v85, s11, v74
	v_sub_f32_e32 v89, s15, v76
	v_sub_f32_e32 v80, v58, v11
	v_sub_f32_e32 v82, v57, v59
	v_sub_f32_e32 v84, v56, v74
	v_sub_f32_e32 v90, v53, v77
	v_sub_f32_e32 v91, s17, v77
	v_sub_f32_e32 v94, v51, v79
	v_sub_f32_e32 v95, s39, v79
	v_mov_b32_e32 v51, v79
	v_mov_b32_e32 v53, v77
	v_mov_b32_e32 v57, v59
	v_mul_f32_e32 v59, 0x3e0293ee, v81
	v_mul_f32_e32 v77, 0x3e0293ee, v83
	v_mul_f32_e32 v79, 0x3e0293ee, v85
	v_mul_f32_e32 v83, 0x3e0293ee, v89
	v_sub_f32_e32 v86, v55, v75
	v_sub_f32_e32 v87, s13, v75
	v_sub_f32_e32 v88, v54, v76
	v_sub_f32_e32 v92, v52, v78
	v_sub_f32_e32 v93, s19, v78
	v_mov_b32_e32 v52, v78
	v_mov_b32_e32 v54, v76
	v_mov_b32_e32 v58, v11
	v_mul_f32_e32 v11, 0x3e0293ee, v80
	v_mul_f32_e32 v78, 0x3e0293ee, v84
	v_exp_f32_e32 v76, v59
	v_exp_f32_e32 v80, v79
	v_exp_f32_e32 v84, v83
	v_mov_b32_e32 v55, v75
	v_mul_f32_e32 v75, 0x3e0293ee, v82
	v_mul_f32_e32 v81, 0x3e0293ee, v86
	v_mul_f32_e32 v85, 0x3e0293ee, v87
	v_mul_f32_e32 v82, 0x3e0293ee, v88
	v_mul_f32_e32 v86, 0x3e0293ee, v90
	v_mul_f32_e32 v87, 0x3e0293ee, v91
	v_mul_f32_e32 v88, 0x3e0293ee, v92
	v_mul_f32_e32 v89, 0x3e0293ee, v93
	v_mul_f32_e32 v90, 0x3e0293ee, v94
	v_mul_f32_e32 v91, 0x3e0293ee, v95
	v_exp_f32_e32 v83, v86
	v_exp_f32_e32 v86, v88
	v_exp_f32_e32 v88, v89
	v_exp_f32_e32 v90, v90
	v_exp_f32_e32 v91, v91
	v_lshlrev_b32_e32 v68, 16, v69
	v_and_b32_e32 v69, 0xffff0000, v69
	v_exp_f32_e32 v78, v78
	v_exp_f32_e32 v79, v81
	v_exp_f32_e32 v82, v82
	v_pk_mul_f32 v[60:61], v[76:77], v[60:61] op_sel_hi:[0,1]
	v_exp_f32_e32 v77, v77
	v_pk_mul_f32 v[64:65], v[80:81], v[64:65] op_sel_hi:[0,1]
	v_exp_f32_e32 v81, v85
	v_pk_mul_f32 v[68:69], v[84:85], v[68:69] op_sel_hi:[0,1]
	v_exp_f32_e32 v85, v87
	v_lshlrev_b32_e32 v62, 16, v15
	v_and_b32_e32 v63, 0xffff0000, v15
	v_lshlrev_b32_e32 v72, 16, v73
	v_and_b32_e32 v73, 0xffff0000, v73
	v_mov_b32_e32 v15, s40
	v_mov_b32_e32 v56, v74
	v_exp_f32_e32 v74, v11
	v_exp_f32_e32 v75, v75
	v_mul_f32_e32 v98, s38, v88
	v_pk_mul_f32 v[72:73], v[88:89], v[72:73] op_sel_hi:[0,1]
	v_pk_mul_f32 v[14:15], v[14:15], v[90:91]
	v_mul_f32_e32 v88, v91, v9
	v_mov_b32_e32 v11, v91
	v_mov_b32_e32 v91, v21
	v_pk_mul_f32 v[10:11], v[10:11], v[90:91]
	v_lshlrev_b32_e32 v70, 16, v71
	v_and_b32_e32 v71, 0xffff0000, v71
	v_mul_f32_e32 v20, v20, v86
	v_mul_f32_e32 v8, v8, v90
	v_mov_b32_e32 v21, v14
	v_mov_b32_e32 v99, v15
	v_pk_fma_f32 v[26:27], v[26:27], v[78:79], v[64:65] op_sel_hi:[1,0,1]
	v_pk_fma_f32 v[18:19], v[18:19], v[82:83], v[68:69] op_sel_hi:[1,0,1]
	v_pk_fma_f32 v[12:13], v[12:13], v[86:87], v[72:73] op_sel_hi:[1,0,1]
	v_mov_b32_e32 v9, v10
	v_mov_b32_e32 v89, v11
	v_mov_b32_e32 v64, v77
	v_pk_mul_f32 v[68:69], s[22:23], v[80:81]
	v_mov_b32_e32 v72, v81
	v_mov_b32_e32 v80, v85
	v_mov_b32_e32 v92, v75
	v_mov_b32_e32 v94, v79
	v_mov_b32_e32 v96, v83
	v_pk_fma_f32 v[32:33], v[32:33], v[74:75], v[60:61] op_sel_hi:[1,0,1]
	v_pk_add_f32 v[20:21], v[20:21], v[98:99]
	v_pk_add_f32 v[8:9], v[8:9], v[88:89]
	v_pk_mul_f32 v[60:61], s[20:21], v[76:77]
	v_pk_mul_f32 v[76:77], s[24:25], v[84:85]
	v_pk_mul_f32 v[62:63], v[64:65], v[62:63] op_sel_hi:[0,1]
	v_pk_mul_f32 v[64:65], v[72:73], v[66:67] op_sel_hi:[0,1]
	v_pk_mul_f32 v[66:67], v[80:81], v[70:71] op_sel_hi:[0,1]
	v_mov_b32_e32 v14, v21
	v_mov_b32_e32 v10, v9
	v_pk_fma_f32 v[36:37], v[36:37], v[74:75], v[60:61]
	v_pk_fma_f32 v[30:31], v[30:31], v[78:79], v[68:69]
	v_pk_fma_f32 v[22:23], v[22:23], v[82:83], v[76:77]
	v_pk_fma_f32 v[28:29], v[28:29], v[92:93], v[62:63] op_sel_hi:[1,0,1]
	v_pk_fma_f32 v[24:25], v[24:25], v[94:95], v[64:65] op_sel_hi:[1,0,1]
	v_pk_fma_f32 v[16:17], v[16:17], v[96:97], v[66:67] op_sel_hi:[1,0,1]
	s_cbranch_scc1 .LBB0_971
	s_waitcnt vmcnt(0)
	s_branch .LBB0_974
